# attention P.V MFMA groups: the compiler's lgkmcnt(0) after the author's counted lgkmcnt(4) relaxed back to lgkmcnt(4) (the eight MFMAs only read the first eight V fragments)
# speedup vs baseline: 1.0017x; 1.0017x over previous
.LBB0_1167:
	v_subrev_u32_e32 v118, s34, v227
	v_subrev_u32_e32 v119, s34, v228
	v_subrev_u32_e32 v120, s34, v229
	v_subrev_u32_e32 v1, s34, v220
	v_subrev_u32_e32 v2, s34, v225
	v_subrev_u32_e32 v5, s34, v226
	s_add_i32 s0, s9, s8
	v_add_u32_e32 v2, s0, v2
	ds_read_b128 v[162:165], v2 offset:57344
	ds_read_b128 v[158:161], v2 offset:59392
	ds_read_b128 v[154:157], v2 offset:61440
	ds_read_b128 v[150:153], v2 offset:63488
	v_add_u32_e32 v2, s0, v5
	v_add_u32_e32 v5, s0, v118
	ds_read_b128 v[146:149], v2
	ds_read_b128 v[142:145], v5
	v_add_u32_e32 v2, s0, v119
	v_add_u32_e32 v1, s0, v1
	v_add_u32_e32 v5, s0, v120
	ds_read_b128 v[138:141], v2
	ds_read_b128 v[134:137], v5
	ds_read_b128 v[118:121], v1 offset:57344
	ds_read_b128 v[122:125], v1 offset:59392
	ds_read_b128 v[126:129], v1 offset:61440
	ds_read_b128 v[130:133], v1 offset:63488
	s_waitcnt lgkmcnt(4)
	s_and_b64 vcc, exec, s[18:19]
	s_cbranch_vccnz .LBB0_1169
	v_pk_mul_f32 v[116:117], v[116:117], v[194:195] op_sel_hi:[1,0]
	v_pk_mul_f32 v[114:115], v[114:115], v[194:195] op_sel_hi:[1,0]
	v_pk_mul_f32 v[112:113], v[112:113], v[194:195] op_sel_hi:[1,0]
	v_pk_mul_f32 v[110:111], v[110:111], v[194:195] op_sel_hi:[1,0]
	v_pk_mul_f32 v[108:109], v[108:109], v[194:195] op_sel_hi:[1,0]
	v_pk_mul_f32 v[106:107], v[106:107], v[194:195] op_sel_hi:[1,0]
	v_pk_mul_f32 v[104:105], v[104:105], v[194:195] op_sel_hi:[1,0]
	v_pk_mul_f32 v[102:103], v[102:103], v[194:195] op_sel_hi:[1,0]
	v_pk_mul_f32 v[100:101], v[100:101], v[194:195] op_sel_hi:[1,0]
	v_pk_mul_f32 v[98:99], v[98:99], v[194:195] op_sel_hi:[1,0]
	v_pk_mul_f32 v[96:97], v[96:97], v[194:195] op_sel_hi:[1,0]
	v_pk_mul_f32 v[94:95], v[94:95], v[194:195] op_sel_hi:[1,0]
	v_pk_mul_f32 v[92:93], v[92:93], v[194:195] op_sel_hi:[1,0]
	v_pk_mul_f32 v[90:91], v[90:91], v[194:195] op_sel_hi:[1,0]
	v_pk_mul_f32 v[88:89], v[88:89], v[194:195] op_sel_hi:[1,0]
	v_pk_mul_f32 v[86:87], v[86:87], v[194:195] op_sel_hi:[1,0]
	s_waitcnt lgkmcnt(4)
	v_mfma_f32_16x16x32_f16 v[114:117], v[162:165], v[38:41], v[114:117]
	v_mfma_f32_16x16x32_f16 v[110:113], v[158:161], v[38:41], v[110:113]
	v_mfma_f32_16x16x32_f16 v[106:109], v[154:157], v[38:41], v[106:109]
	v_mfma_f32_16x16x32_f16 v[102:105], v[150:153], v[38:41], v[102:105]
	v_mfma_f32_16x16x32_f16 v[98:101], v[146:149], v[38:41], v[98:101]
	v_mfma_f32_16x16x32_f16 v[94:97], v[142:145], v[38:41], v[94:97]
	v_mfma_f32_16x16x32_f16 v[90:93], v[138:141], v[38:41], v[90:93]
	v_mfma_f32_16x16x32_f16 v[86:89], v[134:137], v[38:41], v[86:89]
.LBB0_1169:
	v_cndmask_b32_e64 v1, 0, 1, s[76:77]
	v_cmp_ne_u32_e64 s[20:21], 1, v1
	s_andn2_b64 vcc, exec, s[76:77]
	s_cbranch_vccnz .LBB0_1171
	v_pk_mul_f32 v[84:85], v[84:85], v[4:5] op_sel_hi:[1,0]
	v_pk_mul_f32 v[82:83], v[82:83], v[4:5] op_sel_hi:[1,0]
	v_pk_mul_f32 v[80:81], v[80:81], v[4:5] op_sel_hi:[1,0]
	v_pk_mul_f32 v[78:79], v[78:79], v[4:5] op_sel_hi:[1,0]
	v_pk_mul_f32 v[76:77], v[76:77], v[4:5] op_sel_hi:[1,0]
	v_pk_mul_f32 v[74:75], v[74:75], v[4:5] op_sel_hi:[1,0]
	v_pk_mul_f32 v[72:73], v[72:73], v[4:5] op_sel_hi:[1,0]
	v_pk_mul_f32 v[70:71], v[70:71], v[4:5] op_sel_hi:[1,0]
	v_pk_mul_f32 v[68:69], v[68:69], v[4:5] op_sel_hi:[1,0]
	v_pk_mul_f32 v[66:67], v[66:67], v[4:5] op_sel_hi:[1,0]
	v_pk_mul_f32 v[64:65], v[64:65], v[4:5] op_sel_hi:[1,0]
	v_pk_mul_f32 v[62:63], v[62:63], v[4:5] op_sel_hi:[1,0]
	v_pk_mul_f32 v[60:61], v[60:61], v[4:5] op_sel_hi:[1,0]
	v_pk_mul_f32 v[58:59], v[58:59], v[4:5] op_sel_hi:[1,0]
	v_pk_mul_f32 v[56:57], v[56:57], v[4:5] op_sel_hi:[1,0]
	v_pk_mul_f32 v[54:55], v[54:55], v[4:5] op_sel_hi:[1,0]
	s_waitcnt lgkmcnt(4)
	v_mfma_f32_16x16x32_f16 v[82:85], v[162:165], v[46:49], v[82:85]
	v_mfma_f32_16x16x32_f16 v[78:81], v[158:161], v[46:49], v[78:81]
	v_mfma_f32_16x16x32_f16 v[74:77], v[154:157], v[46:49], v[74:77]
	v_mfma_f32_16x16x32_f16 v[70:73], v[150:153], v[46:49], v[70:73]
	v_mfma_f32_16x16x32_f16 v[66:69], v[146:149], v[46:49], v[66:69]
	v_mfma_f32_16x16x32_f16 v[62:65], v[142:145], v[46:49], v[62:65]
	v_mfma_f32_16x16x32_f16 v[58:61], v[138:141], v[46:49], v[58:61]
	v_mfma_f32_16x16x32_f16 v[54:57], v[134:137], v[46:49], v[54:57]

.LBB0_1237:
	v_subrev_u32_e32 v118, s42, v227
	v_subrev_u32_e32 v119, s42, v228
	v_subrev_u32_e32 v120, s42, v229
	v_subrev_u32_e32 v1, s42, v220
	v_subrev_u32_e32 v2, s42, v225
	v_subrev_u32_e32 v5, s42, v226
	s_add_i32 s6, s15, s47
	v_add_u32_e32 v2, s6, v2
	ds_read_b128 v[162:165], v2 offset:57344
	ds_read_b128 v[158:161], v2 offset:59392
	ds_read_b128 v[154:157], v2 offset:61440
	ds_read_b128 v[150:153], v2 offset:63488
	v_add_u32_e32 v2, s6, v5
	v_add_u32_e32 v5, s6, v118
	ds_read_b128 v[146:149], v2
	ds_read_b128 v[142:145], v5
	v_add_u32_e32 v2, s6, v119
	v_add_u32_e32 v1, s6, v1
	v_add_u32_e32 v5, s6, v120
	ds_read_b128 v[138:141], v2
	ds_read_b128 v[134:137], v5
	ds_read_b128 v[118:121], v1 offset:57344
	ds_read_b128 v[122:125], v1 offset:59392
	ds_read_b128 v[126:129], v1 offset:61440
	ds_read_b128 v[130:133], v1 offset:63488
	s_waitcnt lgkmcnt(4)
	s_and_b64 vcc, exec, s[18:19]
	s_cbranch_vccnz .LBB0_1239
	v_pk_mul_f32 v[116:117], v[116:117], v[194:195] op_sel_hi:[1,0]
	v_pk_mul_f32 v[114:115], v[114:115], v[194:195] op_sel_hi:[1,0]
	v_pk_mul_f32 v[112:113], v[112:113], v[194:195] op_sel_hi:[1,0]
	v_pk_mul_f32 v[110:111], v[110:111], v[194:195] op_sel_hi:[1,0]
	v_pk_mul_f32 v[108:109], v[108:109], v[194:195] op_sel_hi:[1,0]
	v_pk_mul_f32 v[106:107], v[106:107], v[194:195] op_sel_hi:[1,0]
	v_pk_mul_f32 v[104:105], v[104:105], v[194:195] op_sel_hi:[1,0]
	v_pk_mul_f32 v[102:103], v[102:103], v[194:195] op_sel_hi:[1,0]
	v_pk_mul_f32 v[100:101], v[100:101], v[194:195] op_sel_hi:[1,0]
	v_pk_mul_f32 v[98:99], v[98:99], v[194:195] op_sel_hi:[1,0]
	v_pk_mul_f32 v[96:97], v[96:97], v[194:195] op_sel_hi:[1,0]
	v_pk_mul_f32 v[94:95], v[94:95], v[194:195] op_sel_hi:[1,0]
	v_pk_mul_f32 v[92:93], v[92:93], v[194:195] op_sel_hi:[1,0]
	v_pk_mul_f32 v[90:91], v[90:91], v[194:195] op_sel_hi:[1,0]
	v_pk_mul_f32 v[88:89], v[88:89], v[194:195] op_sel_hi:[1,0]
	v_pk_mul_f32 v[86:87], v[86:87], v[194:195] op_sel_hi:[1,0]
	s_waitcnt lgkmcnt(4)
	v_mfma_f32_16x16x32_f16 v[114:117], v[162:165], v[38:41], v[114:117]
	v_mfma_f32_16x16x32_f16 v[110:113], v[158:161], v[38:41], v[110:113]
	v_mfma_f32_16x16x32_f16 v[106:109], v[154:157], v[38:41], v[106:109]
	v_mfma_f32_16x16x32_f16 v[102:105], v[150:153], v[38:41], v[102:105]
	v_mfma_f32_16x16x32_f16 v[98:101], v[146:149], v[38:41], v[98:101]
	v_mfma_f32_16x16x32_f16 v[94:97], v[142:145], v[38:41], v[94:97]
	v_mfma_f32_16x16x32_f16 v[90:93], v[138:141], v[38:41], v[90:93]
	v_mfma_f32_16x16x32_f16 v[86:89], v[134:137], v[38:41], v[86:89]
.LBB0_1239:
	v_cndmask_b32_e64 v1, 0, 1, s[36:37]
	v_cmp_ne_u32_e64 s[20:21], 1, v1
	s_andn2_b64 vcc, exec, s[36:37]
	s_cbranch_vccnz .LBB0_1241
	v_pk_mul_f32 v[84:85], v[84:85], v[4:5] op_sel_hi:[1,0]
	v_pk_mul_f32 v[82:83], v[82:83], v[4:5] op_sel_hi:[1,0]
	v_pk_mul_f32 v[80:81], v[80:81], v[4:5] op_sel_hi:[1,0]
	v_pk_mul_f32 v[78:79], v[78:79], v[4:5] op_sel_hi:[1,0]
	v_pk_mul_f32 v[76:77], v[76:77], v[4:5] op_sel_hi:[1,0]
	v_pk_mul_f32 v[74:75], v[74:75], v[4:5] op_sel_hi:[1,0]
	v_pk_mul_f32 v[72:73], v[72:73], v[4:5] op_sel_hi:[1,0]
	v_pk_mul_f32 v[70:71], v[70:71], v[4:5] op_sel_hi:[1,0]
	v_pk_mul_f32 v[68:69], v[68:69], v[4:5] op_sel_hi:[1,0]
	v_pk_mul_f32 v[66:67], v[66:67], v[4:5] op_sel_hi:[1,0]
	v_pk_mul_f32 v[64:65], v[64:65], v[4:5] op_sel_hi:[1,0]
	v_pk_mul_f32 v[62:63], v[62:63], v[4:5] op_sel_hi:[1,0]
	v_pk_mul_f32 v[60:61], v[60:61], v[4:5] op_sel_hi:[1,0]
	v_pk_mul_f32 v[58:59], v[58:59], v[4:5] op_sel_hi:[1,0]
	v_pk_mul_f32 v[56:57], v[56:57], v[4:5] op_sel_hi:[1,0]
	v_pk_mul_f32 v[54:55], v[54:55], v[4:5] op_sel_hi:[1,0]
	s_waitcnt lgkmcnt(4)
	v_mfma_f32_16x16x32_f16 v[82:85], v[162:165], v[46:49], v[82:85]
	v_mfma_f32_16x16x32_f16 v[78:81], v[158:161], v[46:49], v[78:81]
	v_mfma_f32_16x16x32_f16 v[74:77], v[154:157], v[46:49], v[74:77]
	v_mfma_f32_16x16x32_f16 v[70:73], v[150:153], v[46:49], v[70:73]
	v_mfma_f32_16x16x32_f16 v[66:69], v[146:149], v[46:49], v[66:69]
	v_mfma_f32_16x16x32_f16 v[62:65], v[142:145], v[46:49], v[62:65]
	v_mfma_f32_16x16x32_f16 v[58:61], v[138:141], v[46:49], v[58:61]
	v_mfma_f32_16x16x32_f16 v[54:57], v[134:137], v[46:49], v[54:57]
